# scatter: gate load issued together with the expert/rank load (one round trip instead of two)
# speedup vs baseline: 1.0075x; 1.0038x over previous
.LBB0_1354:
	global_load_dword v3, v[4:5], off
	v_add_co_u32_e32 v26, vcc, 0x80000, v4
	s_mov_b64 s[8:9], 0x80000
	s_nop 0
	v_addc_co_u32_e32 v27, vcc, 0, v5, vcc
	v_add_co_u32_e32 v10, vcc, 0x100000, v4
	global_load_dword v28, v[26:27], off
	s_nop 0
	v_addc_co_u32_e32 v11, vcc, 0, v5, vcc
	s_waitcnt vmcnt(1)
	v_and_b32_e32 v7, 0xff, v3
	v_lshl_add_u32 v7, v7, 2, 0
	v_add_u32_e32 v7, 0x20480, v7
	ds_read_b32 v7, v7
	v_lshrrev_b32_e32 v3, 8, v3
	s_waitcnt lgkmcnt(0)
	v_add_u32_e32 v8, v7, v3
	global_store_dword v[10:11], v8, off
	v_lshl_add_u64 v[10:11], v[4:5], 0, s[8:9]
	v_ashrrev_i32_e32 v9, 31, v8
	v_lshlrev_b64 v[4:5], 2, v[8:9]
	v_lshl_add_u64 v[8:9], s[50:51], 0, v[4:5]
	v_lshl_add_u64 v[4:5], s[46:47], 0, v[4:5]
	s_waitcnt vmcnt(1)
	global_store_dword v[8:9], v28, off
	v_ashrrev_i32_e32 v3, 2, v2
	v_add_u32_e32 v2, 0x20000, v2
	v_cmp_le_i32_e32 vcc, s2, v2
	global_store_dword v[4:5], v3, off
	s_or_b64 s[6:7], vcc, s[6:7]
	v_mov_b64_e32 v[4:5], v[10:11]
	s_andn2_b64 exec, exec, s[6:7]
	s_cbranch_execnz .LBB0_1354
